# index_scores: query fragments of heads 8-15 loaded straight from global memory into registers, LDS staging and both workgroup barriers removed from the sub-phase
# baseline (speedup 1.0000x reference)
.LBB0_437:
	s_and_b64 s[6:7], s[4:5], exec
	s_cselect_b32 s18, s16, s17
	s_lshl_b32 s6, s18, 4
	s_add_i32 s20, s6, s19
	s_waitcnt vmcnt(15)
	v_add_u32_e32 v2, s20, v90
	v_mov_b64_e32 v[0:1], s[12:13]
	v_mad_i64_i32 v[2:3], s[6:7], v2, s96, v[0:1]
	v_lshl_add_u64 v[2:3], v[2:3], 0, v[32:33]
	s_waitcnt vmcnt(14)
	v_add_u32_e32 v4, s20, v91
	v_add_co_u32_e32 v2, vcc, s75, v2
	v_mad_i64_i32 v[4:5], s[6:7], v4, s96, v[0:1]
	s_nop 0
	v_addc_co_u32_e32 v3, vcc, 0, v3, vcc
	v_lshl_add_u64 v[4:5], v[4:5], 0, v[32:33]
	v_add_co_u32_e32 v4, vcc, s75, v4
	v_or_b32_e32 v104, s20, v118
	s_nop 0
	v_addc_co_u32_e32 v5, vcc, 0, v5, vcc
	v_mad_i64_i32 v[0:1], s[6:7], v104, s96, v[0:1]
	v_lshlrev_b32_e32 v4, 1, v86
	v_mov_b32_e32 v5, v33
	v_ashrrev_i32_e32 v105, 31, v104
	v_lshl_add_u64 v[0:1], v[0:1], 0, v[4:5]
	v_lshlrev_b64 v[2:3], 10, v[104:105]
	s_mov_b64 s[6:7], 0x8800
	s_waitcnt vmcnt(1)
	v_add_co_u32_e32 v62, vcc, s75, v0
	v_lshl_add_u64 v[2:3], s[14:15], 0, v[2:3]
	s_waitcnt vmcnt(0)
	v_lshl_add_u64 v[66:67], v[0:1], 0, s[6:7]
	v_addc_co_u32_e32 v63, vcc, 0, v1, vcc
	global_load_dwordx4 v[70:73], v[2:3], off offset:560
	global_load_dwordx4 v[74:77], v[2:3], off offset:544
	global_load_dwordx4 v[78:81], v[2:3], off offset:528
	global_load_dwordx4 v[82:85], v[2:3], off offset:512
	s_nop 0
	global_load_dwordx4 v[0:3], v[66:67], off offset:64
	global_load_dwordx4 v[4:7], v[66:67], off offset:128
	global_load_dwordx4 v[8:11], v[66:67], off offset:192
	global_load_dwordx4 v[12:15], v[66:67], off offset:256
	global_load_dwordx4 v[16:19], v[66:67], off offset:320
	global_load_dwordx4 v[20:23], v[66:67], off offset:384
	global_load_dwordx4 v[24:27], v[66:67], off offset:448
	global_load_dwordx4 v[28:31], v[66:67], off offset:512
	global_load_dwordx4 v[38:41], v[66:67], off offset:576
	global_load_dwordx4 v[42:45], v[66:67], off offset:640
	global_load_dwordx4 v[46:49], v[66:67], off offset:704
	global_load_dwordx4 v[50:53], v[66:67], off offset:768
	global_load_dwordx4 v[54:57], v[66:67], off offset:832
	global_load_dwordx4 v[58:61], v[66:67], off offset:896
	global_load_dwordx4 v[140:143], v[66:67], off offset:1024
	global_load_dwordx4 v[144:147], v[66:67], off offset:1088
	global_load_dwordx4 v[148:151], v[66:67], off offset:1152
	global_load_dwordx4 v[152:155], v[66:67], off offset:1216
	global_load_dwordx4 v[156:159], v[66:67], off offset:1280
	global_load_dwordx4 v[160:163], v[66:67], off offset:1344
	global_load_dwordx4 v[164:167], v[66:67], off offset:1408
	global_load_dwordx4 v[168:171], v[66:67], off offset:1472
	global_load_dwordx4 v[172:175], v[66:67], off offset:1536
	global_load_dwordx4 v[176:179], v[66:67], off offset:1600
	global_load_dwordx4 v[180:183], v[66:67], off offset:1664
	global_load_dwordx4 v[184:187], v[66:67], off offset:1728
	global_load_dwordx4 v[188:191], v[66:67], off offset:1792
	global_load_dwordx4 v[192:195], v[66:67], off offset:1856
	global_load_dwordx4 v[196:199], v[66:67], off offset:1920
	global_load_dwordx4 v[200:203], v[66:67], off offset:1984
	s_nop 0
	global_load_dwordx4 v[62:65], v[62:63], off offset:2048
	s_nop 0
	global_load_dwordx4 v[66:69], v[66:67], off offset:960
	s_ashr_i32 s6, s18, 31
	s_lshr_b32 s6, s6, 30
	s_add_i32 s18, s18, s6
	s_and_b32 s7, s18, -4
	s_add_i32 s6, s7, 4
	v_lshl_or_b32 v95, v104, 13, v86
	s_cmp_ge_i32 s8, s6
	s_mov_b32 s18, -1
	s_cbranch_scc1 .LBB0_443
	s_waitcnt vmcnt(35)
	v_mul_f32_e32 v100, 0.5, v70
	v_or_b32_e32 v70, s19, v118
	v_lshl_or_b32 v104, v70, 7, v87
	s_waitcnt vmcnt(32)
	v_mul_f32_e32 v82, 0.5, v82
	v_mul_f32_e32 v83, 0.5, v83
	v_mul_f32_e32 v84, 0.5, v84
	v_mul_f32_e32 v85, 0.5, v85
	v_mul_f32_e32 v78, 0.5, v78
	v_mul_f32_e32 v79, 0.5, v79
	v_mul_f32_e32 v80, 0.5, v80
	v_mul_f32_e32 v81, 0.5, v81
	v_mul_f32_e32 v96, 0.5, v74
	v_mul_f32_e32 v97, 0.5, v75
	v_mul_f32_e32 v98, 0.5, v76
	v_mul_f32_e32 v99, 0.5, v77
	v_mul_f32_e32 v101, 0.5, v71
	v_mul_f32_e32 v102, 0.5, v72
	v_mul_f32_e32 v103, 0.5, v73
	v_add_u32_e32 v107, s10, v104
	v_add_u32_e32 v106, s9, v104
	s_or_b32 s7, s7, 3
	v_or_b32_e32 v105, 64, v104
	s_mov_b32 s21, -1
	s_mov_b32 s20, s11
	s_mov_b32 s19, s8
	global_load_dwordx4 v[132:135], v107, s[2:3]
	global_load_dwordx4 v[136:139], v106, s[2:3]
	s_waitcnt lgkmcnt(0)
